# cq hoist + counted per-k-step vmcnt waits before the fp8 MFMAs
# speedup vs baseline: 1.0218x; 1.0082x over previous
_Z7na_mainPKDF16_PKhS0_PKfS4_S4_S4_Pf:
	s_lshl_b32 s3, s2, 5
	s_and_b32 s3, s3, 0xe0
	s_ashr_i32 s2, s2, 3
	s_add_i32 s3, s3, s2
	s_ashr_i32 s2, s3, 6
	s_lshl_b32 s3, s3, 5
	s_and_b32 s14, s3, 0x7e0
	v_mov_b32_e32 v1, 0x7c0
	s_load_dwordx8 s[4:11], s[0:1], 0x0
	s_load_dwordx2 s[18:19], s[0:1], 0x20
	v_med3_u32 v1, s14, 32, v1
	v_subrev_u32_e32 v97, 32, v1
	s_ashr_i32 s3, s2, 31
	v_lshlrev_b32_e32 v58, 1, v97
	s_lshl_b64 s[12:13], s[2:3], 12
	v_mov_b32_e32 v59, 0
	v_sub_u32_e32 v60, s14, v97
	v_lshl_add_u64 v[10:11], s[12:13], 0, v[58:59]
	v_lshlrev_b64 v[2:3], 9, v[10:11]
	v_lshl_or_b32 v22, v60, 6, v0
	s_waitcnt lgkmcnt(0)
	v_and_b32_e32 v208, 31, v0
	v_lshlrev_b32_e32 v208, 5, v208
	global_load_dwordx4 v[192:195], v208, s[18:19]
	global_load_dwordx4 v[196:199], v208, s[18:19] offset:16
	v_lshl_add_u64 v[20:21], s[4:5], 0, v[2:3]
	v_ashrrev_i32_e32 v23, 31, v22
	v_lshl_add_u64 v[2:3], v[22:23], 4, v[20:21]
	global_load_dwordx4 v[12:15], v[2:3], off
	v_or_b32_e32 v28, 0x200, v22
	v_ashrrev_i32_e32 v29, 31, v28
	v_lshl_add_u64 v[2:3], v[28:29], 4, v[20:21]
	global_load_dwordx4 v[16:19], v[2:3], off
	v_or_b32_e32 v184, 0x400, v22
	v_ashrrev_i32_e32 v185, 31, v184
	v_lshl_add_u64 v[184:185], v[184:185], 4, v[20:21]
	v_or_b32_e32 v188, 0x600, v22
	v_ashrrev_i32_e32 v189, 31, v188
	v_lshl_add_u64 v[188:189], v[188:189], 4, v[20:21]
	global_load_dwordx4 v[184:187], v[184:185], off
	global_load_dwordx4 v[188:191], v[188:189], off
	v_lshrrev_b32_e32 v99, 6, v0
	v_and_b32_e32 v98, 63, v0
	v_lshlrev_b32_e32 v118, 13, v99
	v_lshl_or_b32 v58, v98, 5, v118
	s_movk_i32 s15, 0x1000
	v_lshl_add_u64 v[24:25], s[6:7], 0, v[58:59]
	v_or_b32_e32 v32, 0x400, v22
	v_or_b32_e32 v62, 0x600, v22
	v_add_co_u32_e32 v64, vcc, s15, v24
	s_mov_b64 s[12:13], 0x1000
	s_mov_b64 s[16:17], 0x1800
	v_lshlrev_b32_e32 v72, 1, v60
	v_lshrrev_b32_e32 v23, 5, v22
	v_and_b32_e32 v34, 32, v22
	v_ashrrev_i32_e32 v33, 31, v32
	v_ashrrev_i32_e32 v63, 31, v62
	v_addc_co_u32_e32 v65, vcc, 0, v25, vcc
	global_load_dwordx4 v[6:9], v58, s[6:7] offset:16
	global_load_dwordx4 v[2:5], v58, s[6:7]
	global_load_dwordx4 v[54:57], v58, s[6:7] offset:2064
	global_load_dwordx4 v[50:53], v58, s[6:7] offset:2048
	v_lshrrev_b32_e32 v58, 6, v22
	v_bfe_u32 v73, v22, 8, 2
	v_lshl_add_u64 v[26:27], v[24:25], 0, s[12:13]
	v_lshl_add_u64 v[24:25], v[24:25], 0, s[16:17]
	v_cmp_ne_u32_e32 vcc, 0, v34
	v_sub_u32_e32 v75, v23, v72
	global_load_dwordx4 v[42:45], v[64:65], off
	global_load_dwordx4 v[46:49], v[26:27], off offset:16
	global_load_dwordx4 v[34:37], v[64:65], off offset:2048
	global_load_dwordx4 v[38:41], v[24:25], off offset:16
	v_mov_b32_e32 v61, 0x60
	v_cndmask_b32_e32 v74, 0, v61, vcc
	v_add_u32_e32 v33, v74, v58
	v_lshlrev_b32_e32 v64, 2, v33
	v_bfe_u32 v96, v0, 4, 1
	v_and_b32_e32 v100, 15, v0
	v_mov_b32_e32 v30, v59
	v_mov_b32_e32 v31, v59
	v_and_b32_e32 v64, 12, v64
	v_mul_u32_u24_e32 v29, 0xc000, v96
	v_bitop3_b32 v64, v64, v100, v73 bitop3:0x36
	v_lshl_or_b32 v64, v64, 4, v29
	v_lshlrev_b32_e32 v63, 1, v75
	v_lshl_add_u32 v33, v33, 8, v64
	v_bfe_u32 v71, v0, 1, 4
	v_and_b32_e32 v70, 32, v0
	v_lshlrev_b32_e32 v1, 3, v0
	v_lshrrev_b32_e32 v58, 1, v75
	v_and_b32_e32 v1, 8, v1
	v_add_lshl_u32 v58, v58, v70, 8
	v_lshlrev_b32_e32 v121, 3, v99
	v_bfe_u32 v101, v0, 4, 2
	v_lshlrev_b32_e32 v102, 2, v101
	v_and_b32_e32 v116, 31, v0
	v_bfe_u32 v119, v0, 5, 1
	v_lshlrev_b32_e32 v124, 1, v119
	v_lshlrev_b32_e32 v117, 8, v116
	v_lshrrev_b32_e32 v95, 4, v0
	s_movk_i32 s16, 0x60
	s_mov_b32 s17, 0xc000
	v_and_b32_e32 v211, 3, v99
	v_lshrrev_b32_e32 v212, 2, v99
	v_lshl_or_b32 v211, v211, 2, v212
	v_xor_b32_e32 v213, v100, v211
	v_mul_u32_u24_e32 v214, 0x60, v119
	v_add3_u32 v214, v214, v60, v99
	v_mul_u32_u24_e32 v215, 0xc000, v96
	v_lshl_add_u32 v214, v214, 8, v215
	v_lshl_or_b32 v220, v213, 4, v214
	v_xor_b32_e32 v221, 32, v220
	v_xor_b32_e32 v216, v71, v211
	v_lshl_add_u32 v217, v119, 5, v99
	v_lshlrev_b32_e32 v217, 8, v217
	v_lshl_or_b32 v216, v216, 4, v217
	v_or_b32_e32 v216, v216, v1
	v_add_u32_e32 v222, 0x23800, v216
	v_xor_b32_e32 v223, 32, v222
	s_waitcnt vmcnt(11)
	ds_write_b128 v220, v[12:15]
	v_fma_mix_f32 v200, v192, v12, 0 op_sel_hi:[0,1,0]
	v_fma_mix_f32 v201, v193, v12, 0 op_sel:[0,1,0] op_sel_hi:[0,1,0]
	v_cvt_f32_f16_e32 v211, v12
	v_cvt_f32_f16_sdwa v212, v12 dst_sel:DWORD dst_unused:UNUSED_PAD src0_sel:WORD_1
	v_fma_mix_f32 v200, v194, v13, v200 op_sel_hi:[0,1,0]
	v_fma_mix_f32 v201, v195, v13, v201 op_sel:[0,1,0] op_sel_hi:[0,1,0]
	v_cvt_f32_f16_e32 v213, v13
	v_cvt_f32_f16_sdwa v214, v13 dst_sel:DWORD dst_unused:UNUSED_PAD src0_sel:WORD_1
	v_fma_mix_f32 v200, v196, v14, v200 op_sel_hi:[0,1,0]
	v_fma_mix_f32 v201, v197, v14, v201 op_sel:[0,1,0] op_sel_hi:[0,1,0]
	v_cvt_f32_f16_e32 v215, v14
	v_cvt_f32_f16_sdwa v216, v14 dst_sel:DWORD dst_unused:UNUSED_PAD src0_sel:WORD_1
	v_fma_mix_f32 v200, v198, v15, v200 op_sel_hi:[0,1,0]
	v_fma_mix_f32 v201, v199, v15, v201 op_sel:[0,1,0] op_sel_hi:[0,1,0]
	v_cvt_f32_f16_e32 v217, v15
	v_cvt_f32_f16_sdwa v218, v15 dst_sel:DWORD dst_unused:UNUSED_PAD src0_sel:WORD_1
	v_cvt_pk_fp8_f32 v224, v211, v212
	v_cvt_pk_fp8_f32 v225, v215, v216
	v_cvt_pk_fp8_f32 v224, v213, v214 op_sel:[0,0,1]
	v_cvt_pk_fp8_f32 v225, v217, v218 op_sel:[0,0,1]
	s_nop 0
	ds_write_b64 v222, v[224:225]
	s_waitcnt vmcnt(10)
	ds_write_b128 v221, v[16:19] offset:2048
	v_fma_mix_f32 v202, v192, v16, 0 op_sel_hi:[0,1,0]
	v_fma_mix_f32 v203, v193, v16, 0 op_sel:[0,1,0] op_sel_hi:[0,1,0]
	v_cvt_f32_f16_e32 v211, v16
	v_cvt_f32_f16_sdwa v212, v16 dst_sel:DWORD dst_unused:UNUSED_PAD src0_sel:WORD_1
	v_fma_mix_f32 v202, v194, v17, v202 op_sel_hi:[0,1,0]
	v_fma_mix_f32 v203, v195, v17, v203 op_sel:[0,1,0] op_sel_hi:[0,1,0]
	v_cvt_f32_f16_e32 v213, v17
	v_cvt_f32_f16_sdwa v214, v17 dst_sel:DWORD dst_unused:UNUSED_PAD src0_sel:WORD_1
	v_fma_mix_f32 v202, v196, v18, v202 op_sel_hi:[0,1,0]
	v_fma_mix_f32 v203, v197, v18, v203 op_sel:[0,1,0] op_sel_hi:[0,1,0]
	v_cvt_f32_f16_e32 v215, v18
	v_cvt_f32_f16_sdwa v216, v18 dst_sel:DWORD dst_unused:UNUSED_PAD src0_sel:WORD_1
	v_fma_mix_f32 v202, v198, v19, v202 op_sel_hi:[0,1,0]
	v_fma_mix_f32 v203, v199, v19, v203 op_sel:[0,1,0] op_sel_hi:[0,1,0]
	v_cvt_f32_f16_e32 v217, v19
	v_cvt_f32_f16_sdwa v218, v19 dst_sel:DWORD dst_unused:UNUSED_PAD src0_sel:WORD_1
	v_cvt_pk_fp8_f32 v226, v211, v212
	v_cvt_pk_fp8_f32 v227, v215, v216
	v_cvt_pk_fp8_f32 v226, v213, v214 op_sel:[0,0,1]
	v_cvt_pk_fp8_f32 v227, v217, v218 op_sel:[0,0,1]
	s_nop 0
	ds_write_b64 v223, v[226:227] offset:2048
	s_waitcnt vmcnt(9)
	ds_write_b128 v220, v[184:187] offset:4096
	v_fma_mix_f32 v204, v192, v184, 0 op_sel_hi:[0,1,0]
	v_fma_mix_f32 v205, v193, v184, 0 op_sel:[0,1,0] op_sel_hi:[0,1,0]
	v_cvt_f32_f16_e32 v211, v184
	v_cvt_f32_f16_sdwa v212, v184 dst_sel:DWORD dst_unused:UNUSED_PAD src0_sel:WORD_1
	v_fma_mix_f32 v204, v194, v185, v204 op_sel_hi:[0,1,0]
	v_fma_mix_f32 v205, v195, v185, v205 op_sel:[0,1,0] op_sel_hi:[0,1,0]
	v_cvt_f32_f16_e32 v213, v185
	v_cvt_f32_f16_sdwa v214, v185 dst_sel:DWORD dst_unused:UNUSED_PAD src0_sel:WORD_1
	v_fma_mix_f32 v204, v196, v186, v204 op_sel_hi:[0,1,0]
	v_fma_mix_f32 v205, v197, v186, v205 op_sel:[0,1,0] op_sel_hi:[0,1,0]
	v_cvt_f32_f16_e32 v215, v186
	v_cvt_f32_f16_sdwa v216, v186 dst_sel:DWORD dst_unused:UNUSED_PAD src0_sel:WORD_1
	v_fma_mix_f32 v204, v198, v187, v204 op_sel_hi:[0,1,0]
	v_fma_mix_f32 v205, v199, v187, v205 op_sel:[0,1,0] op_sel_hi:[0,1,0]
	v_cvt_f32_f16_e32 v217, v187
	v_cvt_f32_f16_sdwa v218, v187 dst_sel:DWORD dst_unused:UNUSED_PAD src0_sel:WORD_1
	v_cvt_pk_fp8_f32 v228, v211, v212
	v_cvt_pk_fp8_f32 v229, v215, v216
	v_cvt_pk_fp8_f32 v228, v213, v214 op_sel:[0,0,1]
	v_cvt_pk_fp8_f32 v229, v217, v218 op_sel:[0,0,1]
	s_nop 0
	ds_write_b64 v222, v[228:229] offset:4096
	s_waitcnt vmcnt(8)
	ds_write_b128 v221, v[188:191] offset:6144
	v_fma_mix_f32 v206, v192, v188, 0 op_sel_hi:[0,1,0]
	v_fma_mix_f32 v207, v193, v188, 0 op_sel:[0,1,0] op_sel_hi:[0,1,0]
	v_cvt_f32_f16_e32 v211, v188
	v_cvt_f32_f16_sdwa v212, v188 dst_sel:DWORD dst_unused:UNUSED_PAD src0_sel:WORD_1
	v_fma_mix_f32 v206, v194, v189, v206 op_sel_hi:[0,1,0]
	v_fma_mix_f32 v207, v195, v189, v207 op_sel:[0,1,0] op_sel_hi:[0,1,0]
	v_cvt_f32_f16_e32 v213, v189
	v_cvt_f32_f16_sdwa v214, v189 dst_sel:DWORD dst_unused:UNUSED_PAD src0_sel:WORD_1
	v_fma_mix_f32 v206, v196, v190, v206 op_sel_hi:[0,1,0]
	v_fma_mix_f32 v207, v197, v190, v207 op_sel:[0,1,0] op_sel_hi:[0,1,0]
	v_cvt_f32_f16_e32 v215, v190
	v_cvt_f32_f16_sdwa v216, v190 dst_sel:DWORD dst_unused:UNUSED_PAD src0_sel:WORD_1
	v_fma_mix_f32 v206, v198, v191, v206 op_sel_hi:[0,1,0]
	v_fma_mix_f32 v207, v199, v191, v207 op_sel:[0,1,0] op_sel_hi:[0,1,0]
	v_cvt_f32_f16_e32 v217, v191
	v_cvt_f32_f16_sdwa v218, v191 dst_sel:DWORD dst_unused:UNUSED_PAD src0_sel:WORD_1
	v_cvt_pk_fp8_f32 v230, v211, v212
	v_cvt_pk_fp8_f32 v231, v215, v216
	v_cvt_pk_fp8_f32 v230, v213, v214 op_sel:[0,0,1]
	v_cvt_pk_fp8_f32 v231, v217, v218 op_sel:[0,0,1]
	s_nop 0
	ds_write_b64 v223, v[230:231] offset:6144
	v_add_f32_e32 v200, v200, v201
	v_add_f32_e32 v202, v202, v203
	v_add_f32_e32 v204, v204, v205
	v_add_f32_e32 v206, v206, v207
	v_lshlrev_b32_e32 v208, 7, v119
	v_lshl_add_u32 v208, v99, 2, v208
	v_add_u32_e32 v208, 0x27800, v208
	v_add_f32_dpp v200, v200, v200 quad_perm:[1,0,3,2] row_mask:0xf bank_mask:0xf
	v_add_f32_dpp v202, v202, v202 quad_perm:[1,0,3,2] row_mask:0xf bank_mask:0xf
	v_add_f32_dpp v204, v204, v204 quad_perm:[1,0,3,2] row_mask:0xf bank_mask:0xf
	v_add_f32_dpp v206, v206, v206 quad_perm:[1,0,3,2] row_mask:0xf bank_mask:0xf
	v_add_f32_dpp v200, v200, v200 quad_perm:[2,3,0,1] row_mask:0xf bank_mask:0xf
	v_add_f32_dpp v202, v202, v202 quad_perm:[2,3,0,1] row_mask:0xf bank_mask:0xf
	v_add_f32_dpp v204, v204, v204 quad_perm:[2,3,0,1] row_mask:0xf bank_mask:0xf
	v_add_f32_dpp v206, v206, v206 quad_perm:[2,3,0,1] row_mask:0xf bank_mask:0xf
	v_add_f32_dpp v200, v200, v200 row_half_mirror row_mask:0xf bank_mask:0xf
	v_add_f32_dpp v202, v202, v202 row_half_mirror row_mask:0xf bank_mask:0xf
	v_add_f32_dpp v204, v204, v204 row_half_mirror row_mask:0xf bank_mask:0xf
	v_add_f32_dpp v206, v206, v206 row_half_mirror row_mask:0xf bank_mask:0xf
	v_add_f32_dpp v200, v200, v200 row_mirror row_mask:0xf bank_mask:0xf
	v_add_f32_dpp v202, v202, v202 row_mirror row_mask:0xf bank_mask:0xf
	v_add_f32_dpp v204, v204, v204 row_mirror row_mask:0xf bank_mask:0xf
	v_add_f32_dpp v206, v206, v206 row_mirror row_mask:0xf bank_mask:0xf
	v_add_f32_dpp v200, v200, v200 row_bcast:15 row_mask:0xa bank_mask:0xf
	v_add_f32_dpp v202, v202, v202 row_bcast:15 row_mask:0xa bank_mask:0xf
	v_add_f32_dpp v204, v204, v204 row_bcast:15 row_mask:0xa bank_mask:0xf
	v_add_f32_dpp v206, v206, v206 row_bcast:15 row_mask:0xa bank_mask:0xf
	s_mov_b32 exec_lo, 0xffff0000
	s_mov_b32 exec_hi, 0xffff0000
	ds_write_b32 v208, v200
	ds_write_b32 v208, v202 offset:32
	ds_write_b32 v208, v204 offset:64
	ds_write_b32 v208, v206 offset:96
	s_mov_b64 exec, -1
	v_lshlrev_b32_e32 v201, 7, v99
	v_lshl_or_b32 v201, v119, 4, v201
	global_load_dwordx4 v[184:187], v201, s[10:11]
	global_load_dwordx4 v[188:191], v201, s[10:11] offset:32
	global_load_dwordx4 v[192:195], v201, s[10:11] offset:64
	global_load_dwordx4 v[196:199], v201, s[10:11] offset:96
	v_cmp_lt_i32_e32 vcc, v121, v60
	s_nop 0
	v_mov_b32_e32 v15, v59
	v_cndmask_b32_e64 v12, 32, 0, vcc
	v_add_u32_e32 v16, v12, v121
	v_or_b32_e32 v12, v16, v101
	v_lshlrev_b32_e32 v58, 1, v12
	v_lshrrev_b32_e32 v12, 5, v0
	v_and_b32_e32 v12, 2, v12
	v_bitop3_b32 v14, v102, v100, v12 bitop3:0x36
	v_lshl_add_u64 v[12:13], v[10:11], 0, v[58:59]
	v_lshlrev_b64 v[12:13], 9, v[12:13]
	v_lshlrev_b32_e32 v16, 8, v16
	v_lshl_add_u64 v[12:13], s[4:5], 0, v[12:13]
	v_lshlrev_b32_e32 v14, 4, v14
	v_readfirstlane_b32 s6, v16
	v_add_u32_e32 v17, 0xc000, v16
	v_lshl_add_u64 v[12:13], v[12:13], 0, v[14:15]
	s_mov_b32 m0, s6
	s_mov_b64 s[6:7], 0x100
	v_readfirstlane_b32 s12, v17
	global_load_lds_dwordx4 v[12:13], off
	v_lshl_add_u64 v[12:13], v[12:13], 0, s[6:7]
	s_mov_b32 m0, s12
	v_or_b32_e32 v58, 1, v58
	global_load_lds_dwordx4 v[12:13], off
	v_lshl_add_u64 v[12:13], v[10:11], 0, v[58:59]
	v_lshlrev_b64 v[12:13], 9, v[12:13]
	v_lshl_add_u64 v[12:13], s[4:5], 0, v[12:13]
	v_lshl_add_u64 v[12:13], v[12:13], 0, v[14:15]
	v_add_u32_e32 v14, 0x6000, v16
	v_bfe_u32 v61, v0, 2, 2
	v_readfirstlane_b32 s12, v14
	v_add_u32_e32 v14, 0x12000, v16
	s_mov_b32 m0, s12
	v_readfirstlane_b32 s12, v14
	global_load_lds_dwordx4 v[12:13], off
	v_lshl_add_u64 v[12:13], v[12:13], 0, s[6:7]
	s_mov_b32 m0, s12
	v_add_u32_e32 v18, 0x23800, v117
	global_load_lds_dwordx4 v[12:13], off
	v_or_b32_e32 v12, 4, v121
	v_cmp_lt_i32_e32 vcc, v12, v60
	s_nop 1
	v_cndmask_b32_e64 v13, 32, 0, vcc
	v_add_u32_e32 v16, v13, v12
	v_or_b32_e32 v13, v16, v101
	v_lshlrev_b32_e32 v58, 1, v13
	v_bfe_u32 v12, v12, 2, 2
	v_bitop3_b32 v14, v102, v100, v12 bitop3:0x36
	v_lshl_add_u64 v[12:13], v[10:11], 0, v[58:59]
	v_lshlrev_b64 v[12:13], 9, v[12:13]
	v_lshlrev_b32_e32 v16, 8, v16
	v_lshl_add_u64 v[12:13], s[4:5], 0, v[12:13]
	v_lshlrev_b32_e32 v14, 4, v14
	v_readfirstlane_b32 s12, v16
	v_add_u32_e32 v17, 0xc000, v16
	v_lshl_add_u64 v[12:13], v[12:13], 0, v[14:15]
	s_mov_b32 m0, s12
	v_readfirstlane_b32 s12, v17
	v_or_b32_e32 v58, 1, v58
	global_load_lds_dwordx4 v[12:13], off
	v_lshl_add_u64 v[12:13], v[12:13], 0, s[6:7]
	s_mov_b32 m0, s12
	v_lshl_add_u64 v[10:11], v[10:11], 0, v[58:59]
	global_load_lds_dwordx4 v[12:13], off
	v_lshlrev_b64 v[10:11], 9, v[10:11]
	v_add_u32_e32 v12, 0x6000, v16
	v_lshl_add_u64 v[10:11], s[4:5], 0, v[10:11]
	v_readfirstlane_b32 s4, v12
	v_add_u32_e32 v12, 0x12000, v16
	v_lshl_add_u64 v[10:11], v[10:11], 0, v[14:15]
	s_mov_b32 m0, s4
	v_readfirstlane_b32 s4, v12
	global_load_lds_dwordx4 v[10:11], off
	v_lshl_add_u64 v[10:11], v[10:11], 0, s[6:7]
	s_mov_b32 m0, s4
	s_nop 0
	global_load_lds_dwordx4 v[10:11], off
	s_waitcnt lgkmcnt(0)
	s_barrier
	v_lshlrev_b32_e32 v10, 2, v0
	v_and_b32_e32 v94, 12, v10
	v_or_b32_e32 v120, v94, v61
	v_bitop3_b32 v10, v124, v94, v61 bitop3:0x1e
	v_lshl_or_b32 v14, v10, 4, v18
	v_bitop3_b32 v10, v124, v120, 1 bitop3:0x36
	v_lshl_or_b32 v19, v10, 4, v18
	s_load_dwordx4 s[4:7], s[0:1], 0x20
	s_load_dwordx2 s[12:13], s[0:1], 0x38
	ds_read_b128 v[10:13], v14
	ds_read_b128 v[62:65], v14 offset:8192
	ds_read_b128 v[14:17], v19
	ds_read_b128 v[66:69], v19 offset:8192
	v_bitop3_b32 v19, v124, v120, 4 bitop3:0x36
	v_lshl_or_b32 v19, v19, 4, v18
	v_bitop3_b32 v20, v124, v120, 5 bitop3:0x36
	v_lshl_or_b32 v20, v20, 4, v18
	ds_read_b128 v[70:73], v19
	ds_read_b128 v[78:81], v19 offset:8192
	ds_read_b128 v[74:77], v20
	ds_read_b128 v[82:85], v20 offset:8192
	v_bitop3_b32 v19, v124, v120, 8 bitop3:0x36
	v_lshl_or_b32 v19, v19, 4, v18
	v_bitop3_b32 v20, v124, v120, 9 bitop3:0x36
	v_lshl_or_b32 v20, v20, 4, v18
	ds_read_b128 v[86:89], v19
	ds_read_b128 v[104:107], v19 offset:8192
	ds_read_b128 v[90:93], v20
	ds_read_b128 v[108:111], v20 offset:8192
	v_bitop3_b32 v19, v124, v120, 12 bitop3:0x36
	v_lshl_or_b32 v19, v19, 4, v18
	v_bitop3_b32 v20, v124, v120, 13 bitop3:0x36
	v_lshl_or_b32 v18, v20, 4, v18
	ds_read_b128 v[126:129], v19
	ds_read_b128 v[134:137], v19 offset:8192
	ds_read_b128 v[130:133], v18
	ds_read_b128 v[138:141], v18 offset:8192
	v_mov_b32_e32 v103, 0x7f
	v_lshlrev_b32_e32 v58, 7, v99
	v_or_b32_e32 v122, 0x18000, v117
	s_waitcnt vmcnt(18) lgkmcnt(0)
	v_mfma_scale_f32_32x32x64_f8f6f4 v[18:33], v[2:9], v[10:17], 0, v103, v103 op_sel_hi:[0,0,0]
	v_lshlrev_b32_e32 v125, 3, v119
	v_or_b32_e32 v123, 0x1a000, v117
	v_mfma_scale_f32_32x32x64_f8f6f4 v[2:17], v[2:9], v[62:69], 0, v103, v103 op_sel_hi:[0,0,0]
	v_and_b32_e32 v62, 12, v95
	s_waitcnt vmcnt(16)
	v_mfma_scale_f32_32x32x64_f8f6f4 v[18:33], v[50:57], v[70:77], v[18:33], v103, v103 op_sel_hi:[0,0,0]
	v_mfma_scale_f32_32x32x64_f8f6f4 v[2:17], v[50:57], v[78:85], v[2:17], v103, v103 op_sel_hi:[0,0,0]
	s_brev_b32 s10, 60
	v_lshlrev_b32_e32 v58, 6, v0
	v_and_b32_e32 v58, 0x4000, v58
	v_or3_b32 v63, v122, v58, v125
	v_or3_b32 v58, v123, v58, v125
	s_waitcnt vmcnt(14)
	v_mfma_scale_f32_32x32x64_f8f6f4 v[18:33], v[42:49], v[86:93], v[18:33], v103, v103 op_sel_hi:[0,0,0]
	v_mfma_scale_f32_32x32x64_f8f6f4 v[2:17], v[42:49], v[104:111], v[2:17], v103, v103 op_sel_hi:[0,0,0]
	s_nop 0
	s_waitcnt vmcnt(12)
	v_mfma_scale_f32_32x32x64_f8f6f4 v[2:17], v[34:41], v[134:141], v[2:17], v103, v103 op_sel_hi:[0,0,0]
	v_mfma_scale_f32_32x32x64_f8f6f4 v[18:33], v[34:41], v[126:133], v[18:33], v103, v103 op_sel_hi:[0,0,0]
	s_waitcnt vmcnt(8)
	s_nop 15
	s_nop 1
	v_fma_f32 v2, v2, s10, v184
	v_fma_f32 v3, v3, s10, v185
	v_fma_f32 v4, v4, s10, v186
	v_fma_f32 v5, v5, s10, v187
	v_cvt_pk_f16_f32 v2, v2, v3
	v_cvt_pk_f16_f32 v3, v4, v5
	v_bitop3_b32 v4, v95, v120, 12 bitop3:0x6c
	v_pk_fma_f32 v[18:19], v[18:19], s[10:11], v[184:185] op_sel_hi:[1,0,1]
	v_pk_fma_f32 v[20:21], v[20:21], s[10:11], v[186:187] op_sel_hi:[1,0,1]
	v_lshlrev_b32_e32 v4, 4, v4
	v_cvt_pk_f16_f32 v18, v18, v19
	v_cvt_pk_f16_f32 v19, v20, v21
	v_or_b32_e32 v5, v63, v4
	v_or_b32_e32 v4, v58, v4
	ds_write_b64 v5, v[18:19]
	ds_write_b64 v4, v[2:3]
	v_pk_fma_f32 v[2:3], v[22:23], s[10:11], v[188:189] op_sel_hi:[1,0,1]
	v_pk_fma_f32 v[4:5], v[6:7], s[10:11], v[188:189] op_sel_hi:[1,0,1]
	v_pk_fma_f32 v[6:7], v[24:25], s[10:11], v[190:191] op_sel_hi:[1,0,1]
	v_cvt_pk_f16_f32 v2, v2, v3
	v_cvt_pk_f16_f32 v3, v6, v7
	v_pk_fma_f32 v[6:7], v[8:9], s[10:11], v[190:191] op_sel_hi:[1,0,1]
	v_cvt_pk_f16_f32 v4, v4, v5
	v_cvt_pk_f16_f32 v5, v6, v7
	v_bitop3_b32 v6, v62, v120, 1 bitop3:0x36
	v_lshlrev_b32_e32 v6, 4, v6
	v_or_b32_e32 v7, v63, v6
	ds_write_b64 v7, v[2:3]
	v_or_b32_e32 v2, v58, v6
	ds_write_b64 v2, v[4:5]
	v_pk_fma_f32 v[2:3], v[26:27], s[10:11], v[192:193] op_sel_hi:[1,0,1]
	v_pk_fma_f32 v[6:7], v[28:29], s[10:11], v[194:195] op_sel_hi:[1,0,1]
	v_cvt_pk_f16_f32 v2, v2, v3
	v_pk_fma_f32 v[4:5], v[10:11], s[10:11], v[192:193] op_sel_hi:[1,0,1]
	v_cvt_pk_f16_f32 v3, v6, v7
	v_pk_fma_f32 v[6:7], v[12:13], s[10:11], v[194:195] op_sel_hi:[1,0,1]
	v_cvt_pk_f16_f32 v4, v4, v5
	v_cvt_pk_f16_f32 v5, v6, v7
	v_bitop3_b32 v6, v62, v120, 2 bitop3:0x36
	v_lshlrev_b32_e32 v6, 4, v6
	v_or_b32_e32 v7, v63, v6
	ds_write_b64 v7, v[2:3]
	v_or_b32_e32 v2, v58, v6
	ds_write_b64 v2, v[4:5]
	v_pk_fma_f32 v[2:3], v[30:31], s[10:11], v[196:197] op_sel_hi:[1,0,1]
	v_pk_fma_f32 v[6:7], v[32:33], s[10:11], v[198:199] op_sel_hi:[1,0,1]
	v_cvt_pk_f16_f32 v2, v2, v3
	v_pk_fma_f32 v[4:5], v[14:15], s[10:11], v[196:197] op_sel_hi:[1,0,1]
	v_cvt_pk_f16_f32 v3, v6, v7
	v_pk_fma_f32 v[6:7], v[16:17], s[10:11], v[198:199] op_sel_hi:[1,0,1]
	v_cvt_pk_f16_f32 v4, v4, v5
	v_cvt_pk_f16_f32 v5, v6, v7
	v_bitop3_b32 v6, v62, v120, 3 bitop3:0x36
	v_lshlrev_b32_e32 v6, 4, v6
	v_or_b32_e32 v7, v63, v6
	ds_write_b64 v7, v[2:3]
	v_or_b32_e32 v2, v58, v6
	ds_write_b64 v2, v[4:5]
	s_waitcnt vmcnt(0) lgkmcnt(0)
	s_barrier
	v_and_b32_e32 v236, 1, v101
	v_lshrrev_b32_e32 v237, 1, v101
	v_xor_b32_e32 v237, v237, v236
	v_lshl_or_b32 v236, v236, 1, v237
	v_lshrrev_b32_e32 v27, 8, v0
	v_lshrrev_b32_e32 v3, 3, v0
	v_and_b32_e32 v3, 16, v3
	v_mul_u32_u24_e32 v28, 0x60, v27
	v_lshlrev_b32_e32 v26, 5, v27
	v_or_b32_e32 v146, v3, v100
	v_or_b32_e32 v147, v28, v100
	v_or_b32_e32 v4, v146, v26
	v_lshlrev_b32_e32 v209, 2, v4
	v_add_u32_e32 v209, 0x27800, v209
	v_lshlrev_b32_e32 v4, 8, v4
	v_or_b32_e32 v5, 0x18000, v4
	v_bitop3_b32 v11, v236, v120, 12 bitop3:0x36
	v_or_b32_e32 v95, 0x1c000, v4
	v_lshlrev_b32_e32 v29, 3, v101
	v_bitop3_b32 v6, v236, v94, v61 bitop3:0x1e
	v_bitop3_b32 v8, v236, v120, 4 bitop3:0x36
	v_bitop3_b32 v10, v236, v120, 8 bitop3:0x36
	v_lshlrev_b32_e32 v94, 4, v11
	v_lshlrev_b32_e32 v6, 4, v6
	v_lshlrev_b32_e32 v8, 4, v8
	v_lshlrev_b32_e32 v58, 4, v10
	v_or_b32_e32 v7, v5, v6
	v_or_b32_e32 v9, v5, v8
	v_or_b32_e32 v10, v5, v58
	v_or_b32_e32 v5, v5, v94
	v_or_b32_e32 v6, v95, v6
	v_or_b32_e32 v60, v95, v8
	ds_read_b128 v[22:25], v7
	ds_read_b128 v[18:21], v9
	ds_read_b128 v[14:17], v10
	ds_read_b128 v[10:13], v5
	ds_read_b128 v[6:9], v6
	ds_read_b128 v[2:5], v60
	v_bfe_u32 v103, v0, 6, 1
	s_movk_i32 s5, 0x2000
	v_mad_u32_u24 v44, v103, 48, v147
	v_lshlrev_b32_e32 v60, 8, v44
	v_lshlrev_b32_e32 v44, 2, v44
	v_or_b32_e32 v35, v95, v58
	v_lshlrev_b32_e32 v58, 14, v99
	v_and_b32_e32 v44, 12, v44
	v_or_b32_e32 v56, v44, v61
	v_bitop3_b32 v44, v236, v44, v61 bitop3:0x1e
	v_lshl_add_u64 v[32:33], s[8:9], 0, v[58:59]
	v_lshlrev_b32_e32 v58, 4, v98
	v_or_b32_e32 v36, v95, v94
	v_lshl_add_u64 v[88:89], v[32:33], 0, v[58:59]
	v_lshl_or_b32 v57, v44, 4, v60
	ds_read_b128 v[40:43], v35
	ds_read_b128 v[106:109], v36
	s_load_dword s4, s[6:7], 0x0
	global_load_dwordx4 v[36:39], v[88:89], off
	global_load_dwordx4 v[32:35], v[88:89], off offset:1024
	ds_read_b128 v[44:47], v57
	v_bitop3_b32 v48, v236, v56, 4 bitop3:0x36
	v_lshl_or_b32 v62, v48, 4, v60
	ds_read_b128 v[48:51], v62
	v_bitop3_b32 v52, v236, v56, 8 bitop3:0x36
	v_lshl_or_b32 v63, v52, 4, v60
	ds_read_b128 v[52:55], v63
	s_waitcnt lgkmcnt(0)
	v_mfma_f32_16x16x32_f16 v[44:47], v[44:47], v[22:25], 0
	v_bitop3_b32 v64, v236, v56, 12 bitop3:0x36
	ds_read_b128 v[56:59], v57 offset:49152
	v_lshl_or_b32 v60, v64, 4, v60
	v_mfma_f32_16x16x32_f16 v[44:47], v[48:51], v[18:21], v[44:47]
	ds_read_b128 v[68:71], v60
	ds_read_b128 v[72:75], v62 offset:49152
	v_mad_u32_u24 v104, v103, 3, 1
	v_lshlrev_b32_e32 v132, 4, v104
	v_mfma_f32_16x16x32_f16 v[44:47], v[52:55], v[14:17], v[44:47]
	v_add_u32_e32 v52, v132, v147
	global_load_dwordx4 v[64:67], v[88:89], off offset:2048
	global_load_dwordx4 v[48:51], v[88:89], off offset:3072
	ds_read_b128 v[76:79], v63 offset:49152
	ds_read_b128 v[80:83], v60 offset:49152
	s_waitcnt lgkmcnt(3)
	v_mfma_f32_16x16x32_f16 v[44:47], v[68:71], v[10:13], v[44:47]
	v_lshlrev_b32_e32 v60, 8, v52
	v_lshlrev_b32_e32 v52, 2, v52
	v_and_b32_e32 v52, 12, v52
	v_mfma_f32_16x16x32_f16 v[44:47], v[56:59], v[6:9], v[44:47]
	v_or_b32_e32 v62, v52, v61
	v_bitop3_b32 v52, v236, v52, v61 bitop3:0x1e
	v_lshl_or_b32 v63, v52, 4, v60
	s_waitcnt lgkmcnt(2)
	v_mfma_f32_16x16x32_f16 v[44:47], v[72:75], v[2:5], v[44:47]
	ds_read_b128 v[52:55], v63
	v_bitop3_b32 v56, v236, v62, 4 bitop3:0x36
	v_lshl_or_b32 v84, v56, 4, v60
	s_waitcnt lgkmcnt(2)
	v_mfma_f32_16x16x32_f16 v[44:47], v[76:79], v[40:43], v[44:47]
	ds_read_b128 v[56:59], v84
	v_bitop3_b32 v68, v236, v62, 8 bitop3:0x36
	v_lshl_or_b32 v85, v68, 4, v60
	s_waitcnt lgkmcnt(2)
	v_mfma_f32_16x16x32_f16 v[110:113], v[80:83], v[106:109], v[44:47]
	ds_read_b128 v[68:71], v63 offset:49152
	v_bitop3_b32 v62, v236, v62, 12 bitop3:0x36
	v_lshl_or_b32 v60, v62, 4, v60
	ds_read_b128 v[44:47], v85
	s_waitcnt lgkmcnt(3)
	v_mfma_f32_16x16x32_f16 v[52:55], v[52:55], v[22:25], 0
	ds_read_b128 v[72:75], v60
	ds_read_b128 v[76:79], v84 offset:49152
	v_mad_u32_u24 v105, v103, 3, 2
	v_lshlrev_b32_e32 v133, 4, v105
	s_waitcnt lgkmcnt(4)
	v_mfma_f32_16x16x32_f16 v[52:55], v[56:59], v[18:21], v[52:55]
	ds_read_b128 v[56:59], v85 offset:49152
	v_add_co_u32_e32 v114, vcc, s15, v88
	s_waitcnt lgkmcnt(3)
	v_mfma_f32_16x16x32_f16 v[44:47], v[44:47], v[14:17], v[52:55]
	v_addc_co_u32_e32 v115, vcc, 0, v89, vcc
	s_waitcnt lgkmcnt(2)
	v_mfma_f32_16x16x32_f16 v[44:47], v[72:75], v[10:13], v[44:47]
	ds_read_b128 v[52:55], v60 offset:49152
	v_add_u32_e32 v60, v133, v147
	v_lshlrev_b32_e32 v72, 8, v60
	v_lshlrev_b32_e32 v60, 2, v60
	v_mfma_f32_16x16x32_f16 v[44:47], v[68:71], v[6:9], v[44:47]
	v_and_b32_e32 v60, 12, v60
	v_or_b32_e32 v68, v60, v61
	v_bitop3_b32 v60, v236, v60, v61 bitop3:0x1e
	v_lshl_or_b32 v69, v60, 4, v72
	s_waitcnt lgkmcnt(2)
	v_mfma_f32_16x16x32_f16 v[44:47], v[76:79], v[2:5], v[44:47]
	ds_read_b128 v[60:63], v69
	v_bitop3_b32 v70, v236, v68, 4 bitop3:0x36
	v_lshl_or_b32 v70, v70, 4, v72
	s_waitcnt lgkmcnt(2)
	v_mfma_f32_16x16x32_f16 v[44:47], v[56:59], v[40:43], v[44:47]
	ds_read_b128 v[56:59], v70
	v_bitop3_b32 v71, v236, v68, 8 bitop3:0x36
	v_lshl_or_b32 v71, v71, 4, v72
	s_waitcnt lgkmcnt(1)
	v_mfma_f32_16x16x32_f16 v[22:25], v[60:63], v[22:25], 0
	v_bitop3_b32 v60, v236, v68, 12 bitop3:0x36
	v_lshl_or_b32 v68, v60, 4, v72
	ds_read_b32 v210, v209
	v_mfma_f32_16x16x32_f16 v[126:129], v[52:55], v[106:109], v[44:47]
	s_nop 2
	ds_read_b128 v[44:47], v71
	ds_read_b128 v[52:55], v69 offset:49152
	ds_read_b128 v[60:63], v70 offset:49152
	s_waitcnt lgkmcnt(4)
	v_mfma_f32_16x16x32_f16 v[18:21], v[56:59], v[18:21], v[22:25]
	ds_read_b128 v[56:59], v71 offset:49152
	s_nop 1
	ds_read_b128 v[22:25], v68
	s_waitcnt lgkmcnt(4)
	v_mfma_f32_16x16x32_f16 v[14:17], v[44:47], v[14:17], v[18:21]
	v_add_co_u32_e32 v44, vcc, s5, v88
	s_movk_i32 s5, 0x3000
	s_nop 0
	ds_read_b128 v[18:21], v68 offset:49152
	s_waitcnt lgkmcnt(1)
	v_mfma_f32_16x16x32_f16 v[10:13], v[22:25], v[10:13], v[14:17]
	v_addc_co_u32_e32 v45, vcc, 0, v89, vcc
	global_load_dwordx4 v[84:87], v[114:115], off offset:1024
	global_load_dwordx4 v[80:83], v[114:115], off offset:2048
	global_load_dwordx4 v[92:95], v[44:45], off offset:-4096
	global_load_dwordx4 v[76:79], v[44:45], off
	v_mfma_f32_16x16x32_f16 v[6:9], v[52:55], v[6:9], v[10:13]
	global_load_dwordx4 v[72:75], v[44:45], off offset:1024
	global_load_dwordx4 v[68:71], v[44:45], off offset:2048
	global_load_dwordx4 v[52:55], v[44:45], off offset:3072
	v_mov_b32_e32 v13, 0xff61b1e6
	v_mfma_f32_16x16x32_f16 v[2:5], v[60:63], v[2:5], v[6:9]
	s_nop 2
	v_add_co_u32_e32 v6, vcc, s5, v88
	v_mfma_f32_16x16x32_f16 v[2:5], v[56:59], v[40:43], v[2:5]
	s_nop 0
	v_addc_co_u32_e32 v7, vcc, 0, v89, vcc
	global_load_dwordx4 v[88:91], v[114:115], off offset:3072
	global_load_dwordx4 v[60:63], v[6:7], off
	global_load_dwordx4 v[56:59], v[6:7], off offset:1024
	global_load_dwordx4 v[44:47], v[6:7], off offset:2048
	global_load_dwordx4 v[40:43], v[6:7], off offset:3072
	s_waitcnt lgkmcnt(0)
	v_mfma_f32_16x16x32_f16 v[16:19], v[18:21], v[106:109], v[2:5]
	s_mov_b32 s5, 0xff61b1e6
	s_nop 0
	v_or_b32_e32 v3, s14, v146
	v_mov_b32_e32 v4, 0x7df
	v_med3_u32 v3, v3, 32, v4
	v_or_b32_e32 v4, v97, v102
	v_sub_u32_e32 v3, v4, v3
	v_add_f32_e32 v2, s4, v210
	v_add_u32_e32 v3, 32, v3
	v_mad_u32_u24 v4, v103, 48, v3
	s_movk_i32 s4, 0x41
	v_add_f32_e32 v5, v2, v110
	v_mul_f32_e32 v5, 0x3db8aa3b, v5
	v_cmp_gt_u32_e32 vcc, s4, v4
	v_add_u32_e32 v6, 1, v4
	v_add_f32_e32 v7, v2, v111
	v_cndmask_b32_e32 v5, v13, v5, vcc
	v_mul_f32_e32 v7, 0x3db8aa3b, v7
	v_cmp_gt_u32_e32 vcc, s4, v6
	v_add_u32_e32 v8, 2, v4
	v_add_f32_e32 v9, v2, v112
	v_cndmask_b32_e32 v6, v13, v7, vcc
	v_mul_f32_e32 v9, 0x3db8aa3b, v9
	v_cmp_gt_u32_e32 vcc, s4, v8
	v_add_u32_e32 v4, 3, v4
	v_max3_f32 v7, v5, s5, v6
	v_cndmask_b32_e32 v8, v13, v9, vcc
	v_add_f32_e32 v9, v2, v113
	v_mul_f32_e32 v9, 0x3db8aa3b, v9
	v_cmp_gt_u32_e32 vcc, s4, v4
	v_add_u32_e32 v11, v3, v132
	v_add_f32_e32 v12, v2, v127
	v_cndmask_b32_e32 v10, v13, v9, vcc
	v_max3_f32 v4, v7, v8, v10
	v_add_f32_e32 v7, v2, v126
	v_mul_f32_e32 v7, 0x3db8aa3b, v7
	v_cmp_gt_u32_e32 vcc, s4, v11
	v_add_u32_e32 v9, 1, v11
	v_mul_f32_e32 v12, 0x3db8aa3b, v12
	v_cndmask_b32_e32 v7, v13, v7, vcc
	v_cmp_gt_u32_e32 vcc, s4, v9
	v_add_f32_e32 v14, v2, v128
	v_mul_f32_e32 v14, 0x3db8aa3b, v14
	v_cndmask_b32_e32 v9, v13, v12, vcc
	v_add_u32_e32 v12, 2, v11
	v_cmp_gt_u32_e32 vcc, s4, v12
	v_add_u32_e32 v11, 3, v11
	v_add_u32_e32 v3, v3, v133
	v_cndmask_b32_e32 v12, v13, v14, vcc
	v_add_f32_e32 v14, v2, v129
	v_mul_f32_e32 v14, 0x3db8aa3b, v14
	v_cmp_gt_u32_e32 vcc, s4, v11
	v_add_f32_e32 v11, v2, v16
	v_mul_f32_e32 v11, 0x3db8aa3b, v11
	v_cndmask_b32_e32 v15, v13, v14, vcc
	v_cmp_gt_u32_e32 vcc, s4, v3
	v_add_u32_e32 v14, 1, v3
	v_add_f32_e32 v16, v2, v17
	v_cndmask_b32_e32 v11, v13, v11, vcc
	v_mul_f32_e32 v16, 0x3db8aa3b, v16
	v_cmp_gt_u32_e32 vcc, s4, v14
	v_add_f32_e32 v17, v2, v18
	v_max3_f32 v4, v4, v7, v9
	v_cndmask_b32_e32 v14, v13, v16, vcc
	v_add_u32_e32 v16, 2, v3
	v_mul_f32_e32 v17, 0x3db8aa3b, v17
	v_cmp_gt_u32_e32 vcc, s4, v16
	v_add_u32_e32 v3, 3, v3
	v_add_f32_e32 v2, v2, v19
	v_max3_f32 v4, v4, v12, v15
	v_cndmask_b32_e32 v16, v13, v17, vcc
	v_mul_f32_e32 v2, 0x3db8aa3b, v2
	v_cmp_gt_u32_e32 vcc, s4, v3
	v_max3_f32 v4, v4, v11, v14
	v_lshlrev_b32_e32 v126, 5, v99
	v_cndmask_b32_e32 v17, v13, v2, vcc
	v_max3_f32 v2, v4, v16, v17
	v_mov_b32_e32 v3, v2
	v_lshlrev_b32_e32 v127, 2, v119
	v_lshrrev_b32_e32 v4, 7, v0
	v_cmp_gt_u32_e32 vcc, 16, v98
	v_permlane16_swap_b32_e32 v3, v2
	v_max_f32_e32 v2, v2, v3
	v_mov_b32_e32 v3, v2
	s_nop 1
	v_permlane32_swap_b32_e32 v3, v2
	v_max_f32_e32 v13, v2, v3
	v_and_b32_e32 v2, 0x180, v0
	v_or_b32_e32 v2, 0x23400, v2
	v_lshlrev_b32_e32 v3, 2, v100
	s_and_saveexec_b64 s[4:5], vcc
	v_lshlrev_b32_e32 v18, 6, v103
	v_add3_u32 v18, v2, v18, v3
	ds_write_b32 v18, v13
	s_or_b64 exec, exec, s[4:5]
	v_lshlrev_b32_e32 v18, 4, v103
	v_bitop3_b32 v19, v18, 16, v100 bitop3:0x36
	v_lshl_add_u32 v2, v19, 2, v2
	s_waitcnt lgkmcnt(0)
	s_barrier
	ds_read_b32 v19, v2
	v_max_f32_e32 v13, v13, v13
	v_mul_u32_u24_e32 v20, 0xd00, v4
	s_load_dwordx2 s[0:1], s[0:1], 0x30
	v_or_b32_e32 v2, 1, v124
	s_waitcnt lgkmcnt(0)
	v_max_f32_e32 v19, v19, v19
	v_max_f32_e32 v19, v13, v19
	v_sub_f32_e32 v5, v5, v19
	v_exp_f32_e32 v5, v5
	v_sub_f32_e32 v6, v6, v19
	v_exp_f32_e32 v6, v6
	v_sub_f32_e32 v8, v8, v19
	v_mul_u32_u24_e32 v13, 0xd0, v100
	v_exp_f32_e32 v8, v8
	v_sub_f32_e32 v10, v10, v19
	v_add3_u32 v20, v13, v20, v29
	v_exp_f32_e32 v10, v10
	v_or_b32_e32 v22, 0x20000, v20
	v_add_f32_e32 v20, 0, v5
	v_add_f32_e32 v20, v20, v6
	v_add_f32_e32 v20, v20, v8
	v_add_f32_e32 v23, v20, v10
	v_cvt_pk_f16_f32 v21, v8, v10
	v_cvt_pk_f16_f32 v20, v5, v6
	v_mad_u32_u24 v5, v103, s16, v22
	ds_write_b64 v5, v[20:21]
	v_sub_f32_e32 v5, v7, v19
	v_exp_f32_e32 v5, v5
	v_sub_f32_e32 v6, v9, v19
	v_exp_f32_e32 v6, v6
	v_sub_f32_e32 v7, v12, v19
	v_exp_f32_e32 v7, v7
	v_sub_f32_e32 v8, v15, v19
	v_exp_f32_e32 v8, v8
	v_sub_f32_e32 v10, v11, v19
	v_add_f32_e32 v9, v23, v5
	v_exp_f32_e32 v10, v10
	v_sub_f32_e32 v11, v14, v19
	v_add_f32_e32 v9, v9, v6
	v_exp_f32_e32 v11, v11
	v_sub_f32_e32 v12, v16, v19
	v_add_f32_e32 v9, v9, v7
	v_exp_f32_e32 v12, v12
	v_sub_f32_e32 v14, v17, v19
	v_add_f32_e32 v9, v9, v8
	v_exp_f32_e32 v14, v14
	v_add_f32_e32 v9, v9, v10
	v_add_f32_e32 v9, v9, v11
	v_add_f32_e32 v9, v9, v12
	v_add_f32_e32 v9, v9, v14
	v_mov_b32_e32 v15, v9
	v_cvt_pk_f16_f32 v7, v7, v8
	v_cvt_pk_f16_f32 v6, v5, v6
	v_lshl_add_u32 v5, v104, 5, v22
	ds_write_b64 v5, v[6:7]
	v_permlane16_swap_b32_e32 v15, v9
	v_add_f32_e32 v5, v9, v15
	v_mov_b32_e32 v6, v5
	s_movk_i32 s7, 0xd00
	s_mov_b32 s6, 0x20000
	v_cvt_pk_f16_f32 v9, v12, v14
	v_cvt_pk_f16_f32 v8, v10, v11
	v_lshl_add_u32 v7, v105, 5, v22
	ds_write_b64 v7, v[8:9]
	v_permlane32_swap_b32_e32 v6, v5
	s_and_saveexec_b64 s[4:5], vcc
	s_cbranch_execz .LBB1_4
	v_lshlrev_b32_e32 v4, 5, v4
	v_or_b32_e32 v7, v18, v100
	v_lshlrev_b32_e32 v4, 2, v4
	v_lshlrev_b32_e32 v7, 2, v7
	s_mov_b32 s8, 0x23600
	v_add3_u32 v4, v7, v4, s8
	v_add_f32_e32 v5, v5, v6
	ds_write_b32 v4, v5
